# i4 + grid barrier: XCD leaders no longer forward the release through the per-XCD word nor wait for that atomic and their post-release invalidate before leaving the barrier
# baseline (speedup 1.0000x reference)
.LBB0_795:
	s_or_b64 exec, exec, s[4:5]
	s_waitcnt vmcnt(0)
	buffer_inv sc1
	s_nop 0
	s_nop 0
